# attention output stores as global (not flat) on top of nt H stores + split pk adds
# baseline (speedup 1.0000x reference)
; __device__ __forceinline__ unsigned cvtpk(float lo, float hi) { f32x2_t v = {lo, hi}; bf16x2_t b = __builtin_convertvector(v, bf16x2_t); return __builtin_bit_cast(unsigned, b); }
; __device__ __forceinline__ int crow(int r, int hi) { return (r & 3) + 8 * (r >> 2) + 4 * hi; }
; template <class BIAS>
; __device__ __forceinline__ void attn_tiles(char* shm, const UnitIO& io, int t_begin, int t_end, const BIAS& B, int tid) {
;     ...
;     { auto rr = __builtin_amdgcn_permlane32_swap(__float_as_uint(l_reg), __float_as_uint(l_reg), false, false); l_reg = __uint_as_float(rr[0]) + __uint_as_float(rr[1]); }
;     if (hi == 0) wsf[32 + r32] = l_reg;
;     asm volatile("s_waitcnt lgkmcnt(0)" ::: "memory");
;     float rli[16];
; #pragma unroll
;     for (int r = 0; r < 16; ++r) rli[r] = io.norm ? __builtin_amdgcn_rcpf(wsf[32 + crow(r, hi)]) : 1.0f;
;     if (!io.norm && hi == 0) io.L[(long)r32 * io.lstride] = l_reg;
;     { bf16* stg = (bf16*)(shm + LDS_OST) + wid * 2048;
; #pragma unroll
;       for (int r = 0; r < 16; ++r) { const int orow = crow(r, hi);
; #pragma unroll
;           for (int d0 = 0; d0 < 2; ++d0) stg[orow * 64 + d0 * 32 + r32] = (bf16)(cvtpk(o[d0][r] * rli[r], 0.f) & 0xffffu); }
;       asm volatile("s_waitcnt lgkmcnt(0)" ::: "memory");
; #pragma unroll
;       for (int i = 0; i < 4; ++i) { const int row = i * 8 + (lane >> 3), ch = lane & 7; const u32x4 v = *(const u32x4*)(stg + row * 64 + ch * 8); __builtin_nontemporal_store(v, (u32x4*)(io.O + (long)row * io.ostride + ch * 8)); } }
;     asm volatile("s_waitcnt lgkmcnt(0)" ::: "memory");
.LBB0_277:
	s_or_b64 exec, exec, s[4:5]
	s_waitcnt lgkmcnt(0)
	v_add_u32_e32 v42, s12, v155
	ds_read_b128 v[34:37], v42 offset:128
	ds_read_b128 v[38:41], v42 offset:160
	s_lshl_b64 s[4:5], s[10:11], 1
	v_readlane_b32 s10, v254, 61
	s_add_u32 s4, s10, s4
	s_waitcnt lgkmcnt(1)
	v_rcp_f32_e32 v43, v34
	s_addc_u32 s5, s25, s5
	s_lshl_b32 s10, s16, 12
	s_add_i32 s10, s10, 0x10800
	v_rcp_f32_e32 v44, v35
	v_rcp_f32_e32 v45, v36
	v_rcp_f32_e32 v46, v37
	s_waitcnt lgkmcnt(0)
	v_rcp_f32_e32 v47, v38
	ds_read_b128 v[34:37], v42 offset:192
	v_rcp_f32_e32 v48, v39
	v_rcp_f32_e32 v49, v40
	v_rcp_f32_e32 v50, v41
	ds_read_b128 v[38:41], v42 offset:224
	v_mul_f32_e32 v2, v2, v43
	v_lshl_or_b32 v42, v179, 1, s10
	v_cvt_pk_bf16_f32 v2, v2, s0
	v_lshl_add_u32 v42, v146, 1, v42
	ds_write_b16 v42, v2
	v_mul_f32_e32 v2, v18, v43
	v_cvt_pk_bf16_f32 v2, v2, s0
	ds_write_b16 v42, v2 offset:64
	v_mul_f32_e32 v2, v3, v44
	v_cvt_pk_bf16_f32 v2, v2, s0
	ds_write_b16 v42, v2 offset:128
	v_mul_f32_e32 v2, v19, v44
	v_cvt_pk_bf16_f32 v2, v2, s0
	ds_write_b16 v42, v2 offset:192
	v_mul_f32_e32 v2, v4, v45
	v_cvt_pk_bf16_f32 v2, v2, s0
	ds_write_b16 v42, v2 offset:256
	v_mul_f32_e32 v2, v20, v45
	v_cvt_pk_bf16_f32 v2, v2, s0
	ds_write_b16 v42, v2 offset:320
	v_mul_f32_e32 v2, v5, v46
	v_cvt_pk_bf16_f32 v2, v2, s0
	ds_write_b16 v42, v2 offset:384
	v_mul_f32_e32 v2, v21, v46
	v_cvt_pk_bf16_f32 v2, v2, s0
	ds_write_b16 v42, v2 offset:448
	v_mul_f32_e32 v2, v6, v47
	v_cvt_pk_bf16_f32 v2, v2, s0
	ds_write_b16 v42, v2 offset:1024
	v_mul_f32_e32 v2, v22, v47
	v_cvt_pk_bf16_f32 v2, v2, s0
	ds_write_b16 v42, v2 offset:1088
	v_mul_f32_e32 v2, v7, v48
	v_cvt_pk_bf16_f32 v2, v2, s0
	ds_write_b16 v42, v2 offset:1152
	v_mul_f32_e32 v2, v23, v48
	v_cvt_pk_bf16_f32 v2, v2, s0
	ds_write_b16 v42, v2 offset:1216
	v_mul_f32_e32 v2, v8, v49
	v_cvt_pk_bf16_f32 v2, v2, s0
	ds_write_b16 v42, v2 offset:1280
	v_mul_f32_e32 v2, v24, v49
	v_cvt_pk_bf16_f32 v2, v2, s0
	s_waitcnt lgkmcnt(14)
	v_rcp_f32_e32 v34, v34
	ds_write_b16 v42, v2 offset:1344
	v_mul_f32_e32 v2, v9, v50
	v_cvt_pk_bf16_f32 v2, v2, s0
	ds_write_b16 v42, v2 offset:1408
	v_mul_f32_e32 v2, v25, v50
	v_cvt_pk_bf16_f32 v2, v2, s0
	v_rcp_f32_e32 v35, v35
	ds_write_b16 v42, v2 offset:1472
	v_mul_f32_e32 v2, v10, v34
	v_cvt_pk_bf16_f32 v2, v2, s0
	ds_write_b16 v42, v2 offset:2048
	v_mul_f32_e32 v2, v26, v34
	v_cvt_pk_bf16_f32 v2, v2, s0
	v_rcp_f32_e32 v36, v36
	ds_write_b16 v42, v2 offset:2112
	v_mul_f32_e32 v2, v11, v35
	v_cvt_pk_bf16_f32 v2, v2, s0
	ds_write_b16 v42, v2 offset:2176
	v_mul_f32_e32 v2, v27, v35
	v_cvt_pk_bf16_f32 v2, v2, s0
	v_rcp_f32_e32 v37, v37
	ds_write_b16 v42, v2 offset:2240
	v_mul_f32_e32 v2, v12, v36
	v_cvt_pk_bf16_f32 v2, v2, s0
	ds_write_b16 v42, v2 offset:2304
	v_mul_f32_e32 v2, v28, v36
	v_cvt_pk_bf16_f32 v2, v2, s0
	s_waitcnt lgkmcnt(14)
	v_rcp_f32_e32 v38, v38
	ds_write_b16 v42, v2 offset:2368
	v_mul_f32_e32 v2, v13, v37
	v_cvt_pk_bf16_f32 v2, v2, s0
	ds_write_b16 v42, v2 offset:2432
	v_mul_f32_e32 v2, v29, v37
	v_cvt_pk_bf16_f32 v2, v2, s0
	v_rcp_f32_e32 v39, v39
	ds_write_b16 v42, v2 offset:2496
	v_mul_f32_e32 v2, v14, v38
	v_cvt_pk_bf16_f32 v2, v2, s0
	ds_write_b16 v42, v2 offset:3072
	v_mul_f32_e32 v2, v30, v38
	v_cvt_pk_bf16_f32 v2, v2, s0
	v_rcp_f32_e32 v40, v40
	ds_write_b16 v42, v2 offset:3136
	v_mul_f32_e32 v2, v15, v39
	v_cvt_pk_bf16_f32 v2, v2, s0
	ds_write_b16 v42, v2 offset:3200
	v_mul_f32_e32 v2, v31, v39
	v_cvt_pk_bf16_f32 v2, v2, s0
	v_rcp_f32_e32 v41, v41
	ds_write_b16 v42, v2 offset:3264
	v_mul_f32_e32 v2, v16, v40
	v_cvt_pk_bf16_f32 v2, v2, s0
	ds_write_b16 v42, v2 offset:3328
	v_mul_f32_e32 v2, v32, v40
	v_cvt_pk_bf16_f32 v2, v2, s0
	ds_write_b16 v42, v2 offset:3392
	v_mul_f32_e32 v2, v17, v41
	v_cvt_pk_bf16_f32 v2, v2, s0
	ds_write_b16 v42, v2 offset:3456
	v_mul_f32_e32 v2, v33, v41
	v_cvt_pk_bf16_f32 v2, v2, s0
	v_lshlrev_b32_e32 v152, 1, v160
	ds_write_b16 v42, v2 offset:3520
	v_or_b32_e32 v8, s10, v152
	s_waitcnt lgkmcnt(0)
	v_add_u32_e32 v2, v8, v183
	ds_read_b128 v[2:5], v2
	v_lshl_add_u64 v[6:7], s[4:5], 0, v[0:1]
	v_mov_b32_e32 v153, v1
	v_lshl_add_u64 v[6:7], v[6:7], 0, v[152:153]
	v_mov_b32_e32 v135, v1
	s_waitcnt lgkmcnt(0)
	global_store_dwordx4 v[6:7], v[2:5], off nt
	v_lshl_add_u64 v[6:7], s[4:5], 0, v[134:135]
	v_lshl_add_u64 v[6:7], v[6:7], 0, v[152:153]
	v_add_u32_e32 v2, v8, v185
	ds_read_b128 v[2:5], v2
	v_mov_b32_e32 v137, v1
	v_mov_b32_e32 v139, v1
	s_and_b64 vcc, exec, s[8:9]
	s_waitcnt lgkmcnt(0)
	global_store_dwordx4 v[6:7], v[2:5], off nt
	v_lshl_add_u64 v[6:7], s[4:5], 0, v[136:137]
	s_nop 0
	v_add_u32_e32 v2, v8, v187
	ds_read_b128 v[2:5], v2
	v_lshl_add_u64 v[6:7], v[6:7], 0, v[152:153]
	s_waitcnt lgkmcnt(0)
	global_store_dwordx4 v[6:7], v[2:5], off nt
	s_nop 1
	v_add_u32_e32 v2, v8, v189
	ds_read_b128 v[2:5], v2
	v_lshl_add_u64 v[6:7], s[4:5], 0, v[138:139]
	v_lshl_add_u64 v[6:7], v[6:7], 0, v[152:153]
	s_mov_b64 s[4:5], 0
	s_waitcnt lgkmcnt(0)
	global_store_dwordx4 v[6:7], v[2:5], off nt
	s_waitcnt lgkmcnt(0)
	s_cbranch_vccnz .LBB0_317

; __device__ __forceinline__ unsigned cvtpk(float lo, float hi) { f32x2_t v = {lo, hi}; bf16x2_t b = __builtin_convertvector(v, bf16x2_t); return __builtin_bit_cast(unsigned, b); }
; __device__ __forceinline__ int crow(int r, int hi) { return (r & 3) + 8 * (r >> 2) + 4 * hi; }
; template <class BIAS>
; __device__ __forceinline__ void attn_tiles(char* shm, const UnitIO& io, int t_begin, int t_end, const BIAS& B, int tid) {
;     ...
;     { auto rr = __builtin_amdgcn_permlane32_swap(__float_as_uint(l_reg), __float_as_uint(l_reg), false, false); l_reg = __uint_as_float(rr[0]) + __uint_as_float(rr[1]); }
;     if (hi == 0) wsf[32 + r32] = l_reg;
;     asm volatile("s_waitcnt lgkmcnt(0)" ::: "memory");
;     float rli[16];
; #pragma unroll
;     for (int r = 0; r < 16; ++r) rli[r] = io.norm ? __builtin_amdgcn_rcpf(wsf[32 + crow(r, hi)]) : 1.0f;
;     if (!io.norm && hi == 0) io.L[(long)r32 * io.lstride] = l_reg;
;     { bf16* stg = (bf16*)(shm + LDS_OST) + wid * 2048;
; #pragma unroll
;       for (int r = 0; r < 16; ++r) { const int orow = crow(r, hi);
; #pragma unroll
;           for (int d0 = 0; d0 < 2; ++d0) stg[orow * 64 + d0 * 32 + r32] = (bf16)(cvtpk(o[d0][r] * rli[r], 0.f) & 0xffffu); }
;       asm volatile("s_waitcnt lgkmcnt(0)" ::: "memory");
; #pragma unroll
;       for (int i = 0; i < 4; ++i) { const int row = i * 8 + (lane >> 3), ch = lane & 7; const u32x4 v = *(const u32x4*)(stg + row * 64 + ch * 8); __builtin_nontemporal_store(v, (u32x4*)(io.O + (long)row * io.ostride + ch * 8)); } }
;     asm volatile("s_waitcnt lgkmcnt(0)" ::: "memory");
.LBB0_318:
	s_or_b64 exec, exec, s[42:43]
	s_waitcnt lgkmcnt(0)
	v_lshl_add_u32 v10, v163, 2, s21
	ds_read_b128 v[2:5], v10 offset:128
	ds_read_b128 v[6:9], v10 offset:160
	s_lshl_b64 s[22:23], s[34:35], 1
	v_readlane_b32 s26, v254, 59
	s_add_u32 s22, s26, s22
	v_readlane_b32 s26, v254, 63
	s_addc_u32 s23, s26, s23
	s_lshl_b32 s20, s20, 1
	s_waitcnt lgkmcnt(1)
	v_rcp_f32_e32 v11, v2
	s_add_u32 s34, s22, s20
	s_addc_u32 s35, s23, 0
	s_lshl_b32 s20, s54, 12
	s_add_i32 s20, s20, 0x10800
	v_rcp_f32_e32 v12, v3
	v_rcp_f32_e32 v13, v4
	v_rcp_f32_e32 v14, v5
	s_waitcnt lgkmcnt(0)
	v_rcp_f32_e32 v15, v6
	ds_read_b128 v[2:5], v10 offset:192
	v_rcp_f32_e32 v16, v7
	v_rcp_f32_e32 v17, v8
	v_rcp_f32_e32 v18, v9
	ds_read_b128 v[6:9], v10 offset:224
	v_mul_f32_e32 v10, v202, v11
	v_lshl_or_b32 v19, v179, 1, s20
	v_cvt_pk_bf16_f32 v10, v10, s0
	v_lshl_add_u32 v19, v146, 1, v19
	ds_write_b16 v19, v10
	v_mul_f32_e32 v10, v211, v11
	v_cvt_pk_bf16_f32 v10, v10, s0
	ds_write_b16 v19, v10 offset:64
	v_mul_f32_e32 v10, v200, v12
	v_cvt_pk_bf16_f32 v10, v10, s0
	ds_write_b16 v19, v10 offset:128
	v_mul_f32_e32 v10, v210, v12
	v_cvt_pk_bf16_f32 v10, v10, s0
	ds_write_b16 v19, v10 offset:192
	v_mul_f32_e32 v10, v198, v13
	v_cvt_pk_bf16_f32 v10, v10, s0
	ds_write_b16 v19, v10 offset:256
	v_mul_f32_e32 v10, v209, v13
	v_cvt_pk_bf16_f32 v10, v10, s0
	ds_write_b16 v19, v10 offset:320
	v_mul_f32_e32 v10, v196, v14
	v_cvt_pk_bf16_f32 v10, v10, s0
	ds_write_b16 v19, v10 offset:384
	v_mul_f32_e32 v10, v208, v14
	v_cvt_pk_bf16_f32 v10, v10, s0
	ds_write_b16 v19, v10 offset:448
	v_mul_f32_e32 v10, v176, v15
	v_cvt_pk_bf16_f32 v10, v10, s0
	ds_write_b16 v19, v10 offset:1024
	v_mul_f32_e32 v10, v207, v15
	v_cvt_pk_bf16_f32 v10, v10, s0
	ds_write_b16 v19, v10 offset:1088
	v_mul_f32_e32 v10, v174, v16
	v_cvt_pk_bf16_f32 v10, v10, s0
	ds_write_b16 v19, v10 offset:1152
	v_mul_f32_e32 v10, v206, v16
	v_cvt_pk_bf16_f32 v10, v10, s0
	ds_write_b16 v19, v10 offset:1216
	v_mul_f32_e32 v10, v172, v17
	v_cvt_pk_bf16_f32 v10, v10, s0
	ds_write_b16 v19, v10 offset:1280
	v_mul_f32_e32 v10, v205, v17
	v_cvt_pk_bf16_f32 v10, v10, s0
	s_waitcnt lgkmcnt(14)
	v_rcp_f32_e32 v2, v2
	ds_write_b16 v19, v10 offset:1344
	v_mul_f32_e32 v10, v170, v18
	v_cvt_pk_bf16_f32 v10, v10, s0
	v_rcp_f32_e32 v3, v3
	ds_write_b16 v19, v10 offset:1408
	v_mul_f32_e32 v10, v204, v18
	v_cvt_pk_bf16_f32 v10, v10, s0
	ds_write_b16 v19, v10 offset:1472
	v_mul_f32_e32 v10, v169, v2
	v_mul_f32_e32 v2, v203, v2
	v_cvt_pk_bf16_f32 v2, v2, s0
	v_rcp_f32_e32 v4, v4
	ds_write_b16 v19, v2 offset:2112
	v_mul_f32_e32 v2, v167, v3
	v_cvt_pk_bf16_f32 v2, v2, s0
	ds_write_b16 v19, v2 offset:2176
	v_mul_f32_e32 v2, v201, v3
	v_cvt_pk_bf16_f32 v2, v2, s0
	v_rcp_f32_e32 v5, v5
	ds_write_b16 v19, v2 offset:2240
	v_mul_f32_e32 v2, v153, v4
	v_cvt_pk_bf16_f32 v2, v2, s0
	ds_write_b16 v19, v2 offset:2304
	v_mul_f32_e32 v2, v199, v4
	v_cvt_pk_bf16_f32 v2, v2, s0
	s_waitcnt lgkmcnt(14)
	v_rcp_f32_e32 v6, v6
	ds_write_b16 v19, v2 offset:2368
	v_mul_f32_e32 v2, v149, v5
	v_cvt_pk_bf16_f32 v2, v2, s0
	ds_write_b16 v19, v2 offset:2432
	v_mul_f32_e32 v2, v197, v5
	v_cvt_pk_bf16_f32 v2, v2, s0
	v_rcp_f32_e32 v7, v7
	ds_write_b16 v19, v2 offset:2496
	v_mul_f32_e32 v2, v168, v6
	v_cvt_pk_bf16_f32 v2, v2, s0
	ds_write_b16 v19, v2 offset:3072
	v_mul_f32_e32 v2, v177, v6
	v_cvt_pk_bf16_f32 v2, v2, s0
	v_rcp_f32_e32 v8, v8
	ds_write_b16 v19, v2 offset:3136
	v_mul_f32_e32 v2, v166, v7
	v_cvt_pk_bf16_f32 v2, v2, s0
	ds_write_b16 v19, v2 offset:3200
	v_mul_f32_e32 v2, v175, v7
	v_cvt_pk_bf16_f32 v2, v2, s0
	v_rcp_f32_e32 v9, v9
	ds_write_b16 v19, v2 offset:3264
	v_mul_f32_e32 v2, v151, v8
	v_cvt_pk_bf16_f32 v2, v2, s0
	ds_write_b16 v19, v2 offset:3328
	v_mul_f32_e32 v2, v173, v8
	v_cvt_pk_bf16_f32 v2, v2, s0
	ds_write_b16 v19, v2 offset:3392
	v_mul_f32_e32 v2, v139, v9
	v_cvt_pk_bf16_f32 v2, v2, s0
	ds_write_b16 v19, v2 offset:3456
	v_mul_f32_e32 v2, v171, v9
	v_cvt_pk_bf16_f32 v10, v10, s0
	v_cvt_pk_bf16_f32 v2, v2, s0
	ds_write_b16 v19, v10 offset:2048
	ds_write_b16 v19, v2 offset:3520
	v_or_b32_e32 v8, s20, v152
	s_waitcnt lgkmcnt(0)
	v_add_u32_e32 v2, v8, v183
	ds_read_b128 v[2:5], v2
	v_lshl_add_u64 v[6:7], s[34:35], 0, v[0:1]
	v_mov_b32_e32 v153, v1
	v_lshl_add_u64 v[6:7], v[6:7], 0, v[152:153]
	v_mov_b32_e32 v135, v1
	s_waitcnt lgkmcnt(0)
	global_store_dwordx4 v[6:7], v[2:5], off offset:512 nt
	v_lshl_add_u64 v[6:7], s[34:35], 0, v[134:135]
	v_lshl_add_u64 v[6:7], v[6:7], 0, v[152:153]
	v_add_u32_e32 v2, v8, v185
	ds_read_b128 v[2:5], v2
	v_mov_b32_e32 v137, v1
	v_mov_b32_e32 v139, v1
	s_add_i32 s50, s50, 1
	s_add_i32 s52, s52, 5
	s_waitcnt lgkmcnt(0)
	global_store_dwordx4 v[6:7], v[2:5], off offset:512 nt
	v_lshl_add_u64 v[6:7], s[34:35], 0, v[136:137]
	v_lshl_add_u64 v[6:7], v[6:7], 0, v[152:153]
	v_add_u32_e32 v2, v8, v187
	ds_read_b128 v[2:5], v2
	s_cmp_lg_u32 s50, 3
	s_waitcnt lgkmcnt(0)
	global_store_dwordx4 v[6:7], v[2:5], off offset:512 nt
	s_nop 1
	v_add_u32_e32 v2, v8, v189
	ds_read_b128 v[2:5], v2
	v_lshl_add_u64 v[6:7], s[34:35], 0, v[138:139]
	v_lshl_add_u64 v[6:7], v[6:7], 0, v[152:153]
	s_waitcnt lgkmcnt(0)
	global_store_dwordx4 v[6:7], v[2:5], off offset:512 nt
	s_waitcnt lgkmcnt(0)
	s_cbranch_scc0 .LBB0_361

; __device__ __forceinline__ unsigned cvtpk(float lo, float hi) { f32x2_t v = {lo, hi}; bf16x2_t b = __builtin_convertvector(v, bf16x2_t); return __builtin_bit_cast(unsigned, b); }
; __device__ __forceinline__ int crow(int r, int hi) { return (r & 3) + 8 * (r >> 2) + 4 * hi; }
; template <class BIAS>
; __device__ __forceinline__ void attn_tiles(char* shm, const UnitIO& io, int t_begin, int t_end, const BIAS& B, int tid) {
;     ...
;     { bf16* stg = (bf16*)(shm + LDS_OST) + wid * 2048;
; #pragma unroll
;       for (int r = 0; r < 16; ++r) { const int orow = crow(r, hi);
; #pragma unroll
;           for (int d0 = 0; d0 < 2; ++d0) stg[orow * 64 + d0 * 32 + r32] = (bf16)(cvtpk(o[d0][r] * rli[r], 0.f) & 0xffffu); }
;       asm volatile("s_waitcnt lgkmcnt(0)" ::: "memory");
; #pragma unroll
;       for (int i = 0; i < 4; ++i) { const int row = i * 8 + (lane >> 3), ch = lane & 7; const u32x4 v = *(const u32x4*)(stg + row * 64 + ch * 8); __builtin_nontemporal_store(v, (u32x4*)(io.O + (long)row * io.ostride + ch * 8)); } }
.LBB0_362:
	s_or_b64 exec, exec, s[56:57]
	s_and_b64 s[56:57], s[64:65], exec
	s_movk_i32 s56, 0x1800
	v_readlane_b32 s2, v254, 9
	s_cselect_b32 s64, 0x600, s56
	s_mul_hi_u32 s56, s2, 0x1800000
	s_mul_i32 s57, s2, 0x1800000
	v_readlane_b32 s2, v255, 23
	s_add_u32 s57, s2, s57
	v_readlane_b32 s2, v255, 24
	s_mul_i32 s65, s67, 0x300
	s_mul_hi_u32 s67, s66, 0x300
	s_addc_u32 s56, s2, s56
	s_add_i32 s67, s67, s65
	s_mul_i32 s65, s66, 0x300
	s_add_u32 s57, s57, s65
	v_readlane_b32 s2, v255, 49
	s_addc_u32 s65, s56, s67
	s_lshl_b32 s56, s2, 1
	s_add_u32 s56, s57, s56
	s_addc_u32 s57, s65, 0
	s_lshl_b32 s65, s76, 12
	s_add_i32 s65, s65, 0x10800
	v_cvt_pk_bf16_f32 v0, v2, s0
	v_lshl_or_b32 v2, v179, 1, s65
	v_lshl_add_u32 v2, v146, 1, v2
	ds_write_b16 v2, v0
	v_cvt_pk_bf16_f32 v0, v18, s0
	ds_write_b16 v2, v0 offset:64
	v_cvt_pk_bf16_f32 v0, v3, s0
	ds_write_b16 v2, v0 offset:128
	v_cvt_pk_bf16_f32 v0, v19, s0
	ds_write_b16 v2, v0 offset:192
	v_cvt_pk_bf16_f32 v0, v4, s0
	ds_write_b16 v2, v0 offset:256
	v_cvt_pk_bf16_f32 v0, v20, s0
	ds_write_b16 v2, v0 offset:320
	v_cvt_pk_bf16_f32 v0, v5, s0
	ds_write_b16 v2, v0 offset:384
	v_cvt_pk_bf16_f32 v0, v21, s0
	ds_write_b16 v2, v0 offset:448
	v_cvt_pk_bf16_f32 v0, v6, s0
	ds_write_b16 v2, v0 offset:1024
	v_cvt_pk_bf16_f32 v0, v22, s0
	ds_write_b16 v2, v0 offset:1088
	v_cvt_pk_bf16_f32 v0, v7, s0
	ds_write_b16 v2, v0 offset:1152
	v_cvt_pk_bf16_f32 v0, v23, s0
	ds_write_b16 v2, v0 offset:1216
	v_cvt_pk_bf16_f32 v0, v8, s0
	ds_write_b16 v2, v0 offset:1280
	v_cvt_pk_bf16_f32 v0, v24, s0
	ds_write_b16 v2, v0 offset:1344
	v_cvt_pk_bf16_f32 v0, v9, s0
	ds_write_b16 v2, v0 offset:1408
	v_cvt_pk_bf16_f32 v0, v25, s0
	ds_write_b16 v2, v0 offset:1472
	v_cvt_pk_bf16_f32 v0, v10, s0
	ds_write_b16 v2, v0 offset:2048
	v_cvt_pk_bf16_f32 v0, v26, s0
	ds_write_b16 v2, v0 offset:2112
	v_cvt_pk_bf16_f32 v0, v11, s0
	ds_write_b16 v2, v0 offset:2176
	v_cvt_pk_bf16_f32 v0, v27, s0
	ds_write_b16 v2, v0 offset:2240
	v_cvt_pk_bf16_f32 v0, v12, s0
	ds_write_b16 v2, v0 offset:2304
	v_cvt_pk_bf16_f32 v0, v28, s0
	ds_write_b16 v2, v0 offset:2368
	v_cvt_pk_bf16_f32 v0, v13, s0
	ds_write_b16 v2, v0 offset:2432
	v_cvt_pk_bf16_f32 v0, v29, s0
	ds_write_b16 v2, v0 offset:2496
	v_cvt_pk_bf16_f32 v0, v14, s0
	ds_write_b16 v2, v0 offset:3072
	v_cvt_pk_bf16_f32 v0, v30, s0
	ds_write_b16 v2, v0 offset:3136
	v_cvt_pk_bf16_f32 v0, v15, s0
	ds_write_b16 v2, v0 offset:3200
	v_cvt_pk_bf16_f32 v0, v31, s0
	ds_write_b16 v2, v0 offset:3264
	v_cvt_pk_bf16_f32 v0, v16, s0
	ds_write_b16 v2, v0 offset:3328
	v_cvt_pk_bf16_f32 v0, v32, s0
	ds_write_b16 v2, v0 offset:3392
	v_cvt_pk_bf16_f32 v0, v17, s0
	ds_write_b16 v2, v0 offset:3456
	v_cvt_pk_bf16_f32 v0, v33, s0
	ds_write_b16 v2, v0 offset:3520
	v_or_b32_e32 v8, s65, v152
	s_waitcnt lgkmcnt(0)
	v_add_u32_e32 v0, v8, v183
	s_and_b64 s[62:63], s[62:63], exec
	ds_read_b128 v[2:5], v0
	s_cselect_b32 s62, 0x180, s64
	v_mul_u32_u24_e32 v0, s62, v182
	v_lshlrev_b32_e32 v0, 1, v0
	v_lshl_add_u64 v[6:7], s[56:57], 0, v[0:1]
	v_mov_b32_e32 v153, v1
	v_lshl_add_u64 v[6:7], v[6:7], 0, v[152:153]
	s_waitcnt lgkmcnt(0)
	global_store_dwordx4 v[6:7], v[2:5], off nt
	v_add_u32_e32 v0, v8, v185
	ds_read_b128 v[2:5], v0
	v_mul_u32_u24_e32 v0, s62, v184
	v_lshlrev_b32_e32 v0, 1, v0
	v_lshl_add_u64 v[6:7], s[56:57], 0, v[0:1]
	v_lshl_add_u64 v[6:7], v[6:7], 0, v[152:153]
	s_waitcnt lgkmcnt(0)
	global_store_dwordx4 v[6:7], v[2:5], off nt
	v_add_u32_e32 v0, v8, v187
	ds_read_b128 v[2:5], v0
	v_mul_u32_u24_e32 v0, s62, v186
	v_lshlrev_b32_e32 v0, 1, v0
	v_lshl_add_u64 v[6:7], s[56:57], 0, v[0:1]
	v_lshl_add_u64 v[6:7], v[6:7], 0, v[152:153]
	s_waitcnt lgkmcnt(0)
	global_store_dwordx4 v[6:7], v[2:5], off nt
	v_add_u32_e32 v0, v8, v189
	ds_read_b128 v[2:5], v0
	v_mul_u32_u24_e32 v0, s62, v188
	v_lshlrev_b32_e32 v0, 1, v0
	v_lshl_add_u64 v[6:7], s[56:57], 0, v[0:1]
	v_lshl_add_u64 v[6:7], v[6:7], 0, v[152:153]
	s_waitcnt lgkmcnt(0)
	global_store_dwordx4 v[6:7], v[2:5], off nt
	s_waitcnt lgkmcnt(0)
	s_add_i32 s74, s74, 1
	v_readlane_b32 s3, v254, 10
	s_cmp_eq_u32 s74, 9
	s_cbranch_scc1 .LBB0_393
